# speedup vs baseline: 1.0016x; 1.0016x over previous
_Z11proj_kernelPKfS0_S0_PKDF16_S0_S0_S0_PDF16_S3_S3_Pj:
	s_add_i32 s2, s2, 64
	s_add_i32 s3, s2, 0xffffff40
	s_cmp_ge_u32 s2, 0xc0
	s_cselect_b32 s2, s3, s2
	s_ashr_i32 s12, s2, 6
	s_load_dwordx8 s[4:11], s[0:1], 0x0
	s_cmp_gt_u32 s2, 63
	s_cselect_b64 s[22:23], -1, 0
	s_cmp_lg_u32 s12, 1
	s_cselect_b64 s[18:19], -1, 0
	s_cmp_eq_u32 s12, 1
	s_cselect_b64 s[20:21], -1, 0
	s_and_b64 s[14:15], s[20:21], exec
	s_waitcnt lgkmcnt(0)
	s_cselect_b32 s14, s6, s8
	s_cselect_b32 s15, s7, s9
	s_ashr_i32 s13, s12, 31
	s_lshl_b32 s28, s2, 7
	s_lshl_b64 s[6:7], s[12:13], 19
	s_and_b32 s3, s28, 0x1f80
	s_cmp_lt_u32 s2, 64
	s_cselect_b64 vcc, -1, 0
	v_lshrrev_b32_e32 v1, 2, v0
	v_lshrrev_b32_e32 v2, 2, v0
	v_and_b32_e32 v2, 0x70, v2
	v_bfe_u32 v254, v0, 3, 3
	v_or_b32_e32 v254, v2, v254
	v_or_b32_e32 v2, s3, v254
	s_and_b64 s[8:9], vcc, exec
	s_cselect_b32 s25, s5, s15
	s_cselect_b32 s24, s4, s14
	v_lshlrev_b32_e32 v2, 11, v2
	v_mov_b32_e32 v3, 0
	v_lshlrev_b32_e32 v6, 4, v0
	s_add_u32 s4, s10, s6
	v_lshl_add_u64 v[4:5], s[24:25], 0, v[2:3]
	v_and_b32_e32 v6, 0x70, v6
	v_mov_b32_e32 v7, v3
	v_lshlrev_b32_e32 v56, 4, v0
	v_mov_b32_e32 v57, v3
	s_addc_u32 s5, s11, s7
	v_lshl_add_u64 v[4:5], v[4:5], 0, v[6:7]
	s_mov_b64 s[46:47], 0x4000
	v_lshl_add_u64 v[250:251], v[4:5], 0, s[46:47]
	s_movk_i32 s8, 0x2000
	v_lshl_add_u64 v[6:7], s[4:5], 0, v[56:57]
	global_load_dwordx4 v[8:11], v[4:5], off sc1 nt
	global_load_dwordx4 v[12:15], v[250:251], off sc1 nt
	global_load_dwordx4 v[16:19], v56, s[4:5] sc1
	v_add_co_u32_e64 v28, s[4:5], s8, v6
	s_mov_b32 s33, 0xa000
	s_nop 0
	v_addc_co_u32_e64 v29, s[4:5], 0, v7, s[4:5]
	s_movk_i32 s4, 0x4000
	s_nop 0
	v_add_co_u32_e64 v30, s[4:5], s4, v6
	s_mov_b32 s6, 0xe000
	s_nop 0
	v_addc_co_u32_e64 v31, s[4:5], 0, v7, s[4:5]
	global_load_dwordx4 v[20:23], v[28:29], off sc1
	global_load_dwordx4 v[24:27], v[30:31], off sc1
	s_movk_i32 s4, 0x6000
	v_add_co_u32_e64 v40, s[4:5], s4, v6
	v_lshlrev_b32_e32 v57, 6, v1
	s_nop 0
	v_addc_co_u32_e64 v41, s[4:5], 0, v7, s[4:5]
	global_load_dwordx4 v[28:31], v[40:41], off sc1
	global_load_dwordx4 v[32:35], v[4:5], off offset:128 sc1 nt
	global_load_dwordx4 v[36:39], v[250:251], off offset:128 sc1 nt
	s_mov_b32 s4, 0x8000
	v_add_co_u32_e64 v40, s[4:5], s4, v6
	v_bitop3_b32 v58, v56, 48, v0 bitop3:0x48
	s_nop 0
	v_addc_co_u32_e64 v41, s[4:5], 0, v7, s[4:5]
	v_add_co_u32_e64 v44, s[4:5], s33, v6
	global_load_dwordx4 v[40:43], v[40:41], off sc1
	s_nop 0
	v_addc_co_u32_e64 v45, s[4:5], 0, v7, s[4:5]
	s_mov_b32 s4, 0xc000
	s_nop 0
	v_add_co_u32_e64 v48, s[4:5], s4, v6
	global_load_dwordx4 v[44:47], v[44:45], off sc1
	s_nop 0
	v_addc_co_u32_e64 v49, s[4:5], 0, v7, s[4:5]
	v_add_co_u32_e64 v52, s[4:5], s6, v6
	global_load_dwordx4 v[48:51], v[48:49], off sc1
	s_nop 0
	v_addc_co_u32_e64 v53, s[4:5], 0, v7, s[4:5]
	global_load_dwordx4 v[52:55], v[52:53], off sc1
	s_mov_b32 s4, 0x1e000
	v_bfe_u32 v57, v0, 1, 2
	v_bfe_u32 v58, v254, 2, 2
	v_xor_b32_e32 v57, v57, v58
	v_lshlrev_b32_e32 v57, 4, v57
	v_and_b32_e32 v58, 1, v0
	v_lshl_or_b32 v57, v58, 3, v57
	v_lshl_add_u32 v209, v254, 6, v57
	v_xor_b32_e32 v248, 32, v209
	v_add_u32_e32 v248, 0x200, v248
	v_add_u32_e32 v208, 0, v56
	v_readfirstlane_b32 s30, v0
	v_bfe_u32 v207, v0, 5, 1
	v_bitop3_b32 v1, v207, v1, 3 bitop3:0x78
	v_lshlrev_b32_e32 v210, 4, v1
	s_mov_b32 s34, 0x14000
	v_add_u32_e32 v213, 0x2000, v208
	s_mov_b32 s43, 0
	s_lshr_b32 s29, s30, 6
	s_mov_b32 s35, -2
	s_mov_b32 s36, 0xffff2000
	s_mov_b32 s37, 0xffff4000
	s_mov_b32 s38, 0xffff6000
	s_movk_i32 s39, 0x8000
	s_movk_i32 s40, 0xa000
	s_movk_i32 s41, 0xc000
	s_movk_i32 s42, 0xe000
	s_mov_b64 s[26:27], 0x100
	v_mov_b32_e32 v56, v3
	v_mov_b32_e32 v57, v3
	v_mov_b32_e32 v58, v3
	v_mov_b32_e32 v59, v3
	v_mov_b32_e32 v60, v3
	v_mov_b32_e32 v61, v3
	v_mov_b32_e32 v62, v3
	v_mov_b32_e32 v63, v3
	v_mov_b32_e32 v64, v3
	v_mov_b32_e32 v65, v3
	v_mov_b32_e32 v66, v3
	v_mov_b32_e32 v67, v3
	v_mov_b32_e32 v68, v3
	v_mov_b32_e32 v69, v3
	v_mov_b32_e32 v70, v3
	s_waitcnt vmcnt(11)
	v_cvt_pk_f16_f32 v8, v8, v9
	v_cvt_pk_f16_f32 v9, v10, v11
	s_waitcnt vmcnt(10)
	v_cvt_pk_f16_f32 v10, v12, v13
	v_cvt_pk_f16_f32 v11, v14, v15
	ds_write_b64 v209, v[8:9]
	ds_write_b64 v248, v[10:11]
	v_and_b32_e32 v10, 31, v0
	s_waitcnt vmcnt(9)
	ds_write_b128 v208, v[16:19] offset:8192
	s_waitcnt vmcnt(8)
	ds_write_b128 v208, v[20:23] offset:16384
	s_waitcnt vmcnt(7)
	ds_write_b128 v208, v[24:27] offset:24576
	s_load_dwordx2 s[16:17], s[0:1], 0x50
	s_load_dwordx4 s[12:15], s[0:1], 0x40
	s_load_dwordx8 s[4:11], s[0:1], 0x20
	s_lshl_b32 s0, s30, 1
	s_and_b32 s31, s0, 0x180
	s_lshr_b32 s0, s30, 2
	v_bfe_u32 v11, v0, 2, 2
	s_and_b32 s0, s0, 0x3fffffc0
	s_waitcnt vmcnt(5)
	v_cvt_pk_f16_f32 v8, v32, v33
	v_cvt_pk_f16_f32 v9, v34, v35
	v_or_b32_e32 v12, s31, v10
	v_or_b32_e32 v206, s0, v10
	v_bitop3_b32 v1, v207, v11, 2 bitop3:0x36
	s_waitcnt vmcnt(4)
	v_cvt_pk_f16_f32 v10, v36, v37
	v_cvt_pk_f16_f32 v11, v38, v39
	s_mov_b32 s0, 0x10000
	ds_write_b128 v208, v[28:31] offset:32768
	ds_write_b64 v209, v[8:9] offset:40960
	ds_write_b64 v248, v[10:11] offset:40960
	v_add_co_u32_e64 v8, s[0:1], s0, v6
	global_load_dwordx4 v[154:157], v[250:251], off offset:256 sc1 nt
	global_load_dwordx4 v[162:165], v[4:5], off offset:256 sc1 nt
	v_addc_co_u32_e64 v9, s[0:1], 0, v7, s[0:1]
	s_mov_b32 s0, 0x12000
	global_load_dwordx4 v[158:161], v[8:9], off sc1
	v_add_co_u32_e64 v8, s[0:1], s0, v6
	v_lshl_add_u32 v211, v12, 6, 0
	s_nop 0
	v_addc_co_u32_e64 v9, s[0:1], 0, v7, s[0:1]
	v_add_co_u32_e64 v10, s[0:1], s34, v6
	v_add_u32_e32 v14, 0x12000, v208
	s_nop 0
	v_addc_co_u32_e64 v11, s[0:1], 0, v7, s[0:1]
	s_mov_b32 s0, 0x16000
	s_nop 0
	v_add_co_u32_e64 v12, s[0:1], s0, v6
	s_waitcnt vmcnt(3)
	ds_write_b128 v14, v[52:55]
	v_addc_co_u32_e64 v13, s[0:1], 0, v7, s[0:1]
	s_mov_b32 s0, 0x18000
	s_nop 0
	v_add_co_u32_e64 v14, s[0:1], s0, v6
	ds_write_b128 v208, v[40:43] offset:49152
	s_nop 0
	v_addc_co_u32_e64 v15, s[0:1], 0, v7, s[0:1]
	s_mov_b32 s0, 0x1a000
	s_nop 0
	v_add_co_u32_e64 v16, s[0:1], s0, v6
	ds_write_b128 v208, v[44:47] offset:57344
	s_nop 0
	v_addc_co_u32_e64 v17, s[0:1], 0, v7, s[0:1]
	s_mov_b32 s0, 0x1c000
	ds_write_b128 v213, v[48:51] offset:57344
	v_add_co_u32_e64 v18, s[0:1], s0, v6
	v_add_u32_e32 v216, v211, v210
	s_nop 0
	v_addc_co_u32_e64 v19, s[0:1], 0, v7, s[0:1]
	global_load_dwordx4 v[174:177], v[8:9], off sc1
	global_load_dwordx4 v[166:169], v[10:11], off sc1
	global_load_dwordx4 v[170:173], v[12:13], off sc1
	global_load_dwordx4 v[142:145], v[250:251], off offset:384 sc1 nt
	global_load_dwordx4 v[150:153], v[4:5], off offset:384 sc1 nt
	global_load_dwordx4 v[138:141], v[14:15], off sc1
	global_load_dwordx4 v[146:149], v[16:17], off sc1
	global_load_dwordx4 v[134:137], v[18:19], off sc1
	s_mov_b32 s0, 0x1e000
	v_add_co_u32_e64 v8, s[0:1], s0, v6
	s_nop 1
	v_addc_co_u32_e64 v9, s[0:1], 0, v7, s[0:1]
	global_load_dwordx4 v[130:133], v[8:9], off sc1
	s_waitcnt lgkmcnt(0)
	s_barrier
	v_lshl_add_u32 v218, v206, 6, 0
	v_add_u32_e32 v217, v218, v210
	ds_read_b128 v[198:201], v216 offset:8192
	ds_read_b128 v[194:197], v216 offset:10240
	ds_read_b128 v[190:193], v216 offset:12288
	ds_read_b128 v[178:181], v216 offset:14336
	ds_read_b128 v[186:189], v217
	ds_read_b128 v[182:185], v217 offset:2048
	v_and_b32_e32 v20, 7, v0
	v_lshl_or_b32 v2, v20, 4, v2
	s_mov_b64 s[0:1], 0x2e000
	v_lshlrev_b32_e32 v212, 4, v1
	v_lshl_add_u64 v[202:203], v[6:7], 0, s[0:1]
	s_mov_b64 s[0:1], 0x290
	v_lshl_add_u64 v[4:5], s[24:25], 0, v[2:3]
	v_lshl_add_u64 v[204:205], v[4:5], 0, s[0:1]
	v_lshl_add_u64 v[252:253], v[204:205], 0, s[46:47]
	s_mov_b64 s[24:25], 0x10000
	v_mov_b32_e32 v2, v3
	v_mov_b32_e32 v4, v3
	v_mov_b32_e32 v5, v3
	v_mov_b32_e32 v6, v3
	v_mov_b32_e32 v7, v3
	v_mov_b32_e32 v8, v3
	v_mov_b32_e32 v9, v3
	v_mov_b32_e32 v10, v3
	v_mov_b32_e32 v11, v3
	v_mov_b32_e32 v12, v3
	v_mov_b32_e32 v13, v3
	v_mov_b32_e32 v14, v3
	v_mov_b32_e32 v15, v3
	v_mov_b32_e32 v16, v3
	v_mov_b32_e32 v17, v3
	v_mov_b32_e32 v18, v3
	v_mov_b32_e32 v19, v3
	v_mov_b32_e32 v20, v3
	v_mov_b32_e32 v21, v3
	v_mov_b32_e32 v22, v3
	v_mov_b32_e32 v23, v3
	v_mov_b32_e32 v24, v3
	v_mov_b32_e32 v25, v3
	v_mov_b32_e32 v26, v3
	v_mov_b32_e32 v27, v3
	v_mov_b32_e32 v28, v3
	v_mov_b32_e32 v29, v3
	v_mov_b32_e32 v30, v3
	v_mov_b32_e32 v31, v3
	v_mov_b32_e32 v32, v3
	v_mov_b32_e32 v33, v3
	v_mov_b32_e32 v34, v3
	v_mov_b32_e32 v35, v3
	v_mov_b32_e32 v36, v3
	v_mov_b32_e32 v37, v3
	v_mov_b32_e32 v38, v3
	v_mov_b32_e32 v39, v3
	v_mov_b32_e32 v40, v3
	v_mov_b32_e32 v41, v3
	v_mov_b32_e32 v42, v3
	v_mov_b32_e32 v43, v3
	v_mov_b32_e32 v44, v3
	v_mov_b32_e32 v45, v3
	v_mov_b32_e32 v46, v3
	v_mov_b32_e32 v47, v3
	v_mov_b32_e32 v48, v3
	v_mov_b32_e32 v49, v3
	v_mov_b32_e32 v50, v3
	v_mov_b32_e32 v51, v3
	v_mov_b32_e32 v52, v3
	v_mov_b32_e32 v53, v3
	v_mov_b32_e32 v54, v3
	v_mov_b32_e32 v55, v3
	v_mov_b32_e32 v71, v3
	v_mov_b32_e32 v72, v3
	v_mov_b32_e32 v73, v3
	v_mov_b32_e32 v74, v3
	v_mov_b32_e32 v75, v3
	v_mov_b32_e32 v76, v3
	v_mov_b32_e32 v77, v3
	v_mov_b32_e32 v78, v3
	v_mov_b32_e32 v79, v3
	v_mov_b32_e32 v80, v3
	v_mov_b32_e32 v81, v3
	v_mov_b32_e32 v82, v3
	v_mov_b32_e32 v83, v3
	v_mov_b32_e32 v84, v3
	v_mov_b32_e32 v85, v3
	v_mov_b32_e32 v86, v3
	v_mov_b32_e32 v87, v3
	v_mov_b32_e32 v88, v3
	v_mov_b32_e32 v89, v3
	v_mov_b32_e32 v90, v3
	v_mov_b32_e32 v91, v3
	v_mov_b32_e32 v92, v3
	v_mov_b32_e32 v93, v3
	v_mov_b32_e32 v94, v3
	v_mov_b32_e32 v95, v3
	v_mov_b32_e32 v96, v3
	v_mov_b32_e32 v97, v3
	v_mov_b32_e32 v98, v3
	v_mov_b32_e32 v99, v3
	v_mov_b32_e32 v100, v3
	v_mov_b32_e32 v101, v3
	v_mov_b32_e32 v102, v3
	v_mov_b32_e32 v103, v3
	v_mov_b32_e32 v104, v3
	v_mov_b32_e32 v105, v3
	v_mov_b32_e32 v106, v3
	v_mov_b32_e32 v107, v3
	v_mov_b32_e32 v108, v3
	v_mov_b32_e32 v109, v3
	v_mov_b32_e32 v110, v3
	v_mov_b32_e32 v111, v3
	v_mov_b32_e32 v112, v3
	v_mov_b32_e32 v113, v3
	v_mov_b32_e32 v114, v3
	v_mov_b32_e32 v115, v3
	v_mov_b32_e32 v116, v3
	v_mov_b32_e32 v117, v3
	v_mov_b32_e32 v118, v3
	v_mov_b32_e32 v119, v3
	v_mov_b32_e32 v120, v3
	v_mov_b32_e32 v121, v3
	v_mov_b32_e32 v122, v3
	v_mov_b32_e32 v123, v3
	v_mov_b32_e32 v124, v3
	v_mov_b32_e32 v125, v3
	v_mov_b32_e32 v126, v3
	v_mov_b32_e32 v127, v3
	v_mov_b32_e32 v128, v3
	v_mov_b32_e32 v129, v3
	v_and_b32_e32 v1, 63, v0
	v_add_u32_e32 v215, v211, v212
	v_add_u32_e32 v214, v218, v212
